# baseline (speedup 1.0000x reference)
.Lat_spec_ok:
	v_and_b32_e32 v31, 7, v0
	v_bitop3_b32 v33, v10, v0, 7 bitop3:0x78
	v_lshlrev_b32_e32 v1, 7, v1
	v_mbcnt_lo_u32_b32 v34, -1, 0
	v_lshlrev_b32_e32 v89, 4, v33
	v_bitop3_b32 v31, v10, v31, 4 bitop3:0x36
	v_xor_b32_e32 v33, v13, v0
	v_mov_b32_e32 v13, v12
	v_lshlrev_b32_e32 v87, 4, v11
	s_movk_i32 s1, 0x70
	v_lshlrev_b32_e32 v98, 2, v10
	v_mov_b32_e32 v10, v12
	v_mov_b32_e32 v11, v12
	v_mbcnt_hi_u32_b32 v0, -1, v34
	v_lshl_or_b32 v91, v31, 4, v1
	v_lshlrev_b32_e32 v31, 4, v33
	v_mov_b64_e32 v[36:37], v[12:13]
	v_mov_b64_e32 v[40:41], v[12:13]
	v_mov_b64_e32 v[44:45], v[12:13]
	v_mov_b64_e32 v[48:49], v[12:13]
	v_mov_b64_e32 v[52:53], v[12:13]
	s_mov_b32 s17, 0
	v_mov_b64_e32 v[100:101], 0
	s_mov_b64 s[14:15], -1
	s_mov_b32 s5, 0xff800000
	s_mov_b32 s7, 0x41000000
	s_mov_b32 s12, 0x3c003c00
	v_mov_b32_e32 v30, 0x3c003c00
	v_mov_b32_e32 v114, v30
	v_mov_b32_e32 v115, v30
	v_mov_b32_e32 v116, v30
	v_mov_b32_e32 v117, v30
	v_mov_b32_e32 v120, v12
	v_mov_b32_e32 v121, v12
	v_mov_b32_e32 v122, v12
	v_mov_b32_e32 v123, v12
	v_mov_b64_e32 v[34:35], v[10:11]
	v_mov_b64_e32 v[38:39], v[10:11]
	v_mov_b64_e32 v[42:43], v[10:11]
	v_mov_b64_e32 v[46:47], v[10:11]
	v_mov_b64_e32 v[50:51], v[10:11]
	v_and_or_b32 v99, v31, s1, v32
	s_mov_b32 s9, 0
	s_waitcnt vmcnt(3)
	ds_write_b128 v99, v[22:25]
	ds_write_b128 v90, v[14:17] offset:8192
	s_waitcnt vmcnt(2)
	ds_write_b128 v99, v[18:21] offset:4096
	s_waitcnt vmcnt(1)
	ds_write_b128 v90, v[26:29] offset:12288
	s_waitcnt vmcnt(0)
	s_cmp_gt_i32 s11, 3
	s_cbranch_scc0 .LBB1_20

.LBB1_27:
	s_waitcnt lgkmcnt(0)
	s_barrier
	s_lshl_b32 s10, s9, 14
	s_lshl_b32 s13, 1, s0
	s_and_b32 s0, s13, s4
	v_or_b32_e32 v10, s10, v89
	s_cmp_eq_u32 s0, 0
	v_add_u32_e32 v106, v10, v1
	v_add_u32_e32 v105, s10, v91
	s_cbranch_scc1 .LBB1_32
	ds_read_b128 v[58:61], v106
	ds_read_b128 v[62:65], v105
	v_lshrrev_b64 v[10:11], v98, v[102:103]
	v_bfe_i32 v13, v10, 1, 1
	v_bfe_i32 v31, v10, 2, 1
	s_waitcnt lgkmcnt(1)
	v_mfma_f32_16x16x32_f16 v[58:61], v[58:61], v[2:5], v[120:123]
	v_bfe_i32 v32, v10, 3, 1
	v_bfe_i32 v11, v10, 0, 1
	s_waitcnt lgkmcnt(0)
	v_mfma_f32_16x16x32_f16 v[58:61], v[62:65], v[6:9], v[58:61]
	s_nop 7
	v_bitop3_b32 v10, v59, s5, v13 bitop3:0xe4
	v_bitop3_b32 v31, v60, s5, v31 bitop3:0xe4
	v_bitop3_b32 v13, v61, s5, v32 bitop3:0xe4
	v_max_f32_e32 v32, v13, v13
	v_max_f32_e32 v33, v31, v31
	v_bitop3_b32 v11, v58, s5, v11 bitop3:0xe4
	v_max_f32_e32 v32, v33, v32
	v_max3_f32 v32, v11, v10, v32
	v_cmp_lt_f32_e32 vcc, s7, v32
	s_or_b64 s[0:1], s[14:15], vcc
	s_cbranch_scc0 .LBB1_35
	v_and_b32_e32 v58, 64, v0
	v_xor_b32_e32 v33, 16, v0
	v_add_u32_e32 v58, 64, v58
	v_cmp_lt_i32_e32 vcc, v33, v58
	s_mov_b64 s[22:23], 0
	s_nop 0
	v_cndmask_b32_e32 v33, v0, v33, vcc
	v_lshlrev_b32_e32 v33, 2, v33
	ds_bpermute_b32 v33, v33, v32
	v_max_f32_e32 v32, v32, v32
	s_waitcnt lgkmcnt(0)
	v_max_f32_e32 v33, v33, v33
	v_max_f32_e32 v32, v32, v33
	v_mov_b32_e32 v33, v32
	s_nop 1
	v_permlane32_swap_b32_e32 v32, v33
	v_max_f32_e32 v33, v33, v33
	v_max_f32_e32 v32, v32, v32
	v_max_f32_e32 v32, v32, v33
	v_cmp_nlg_f32_e32 vcc, s5, v32
	v_cmp_lg_f32_e64 s[0:1], s5, v32
	s_and_saveexec_b64 s[24:25], s[0:1]
	v_cmp_lt_f32_e64 s[0:1], s7, v32
	s_or_b64 s[0:1], s[14:15], s[0:1]
	s_and_b64 s[22:23], s[0:1], exec
	s_or_b64 exec, exec, s[24:25]
	v_exp_f32_e64 v33, -v32
	v_cndmask_b32_e64 v32, 0, v32, s[22:23]
	v_sub_f32_e32 v11, v11, v32
	v_sub_f32_e32 v10, v10, v32
	v_cndmask_b32_e64 v33, v33, 1.0, s[14:15]
	v_cndmask_b32_e64 v66, 1.0, v33, s[22:23]
	v_pk_mul_f32 v[60:61], v[48:49], v[66:67] op_sel_hi:[1,0]
	v_pk_mul_f32 v[58:59], v[46:47], v[66:67] op_sel_hi:[1,0]
	v_pk_mul_f32 v[64:65], v[66:67], v[44:45] op_sel_hi:[0,1]
	v_pk_mul_f32 v[62:63], v[66:67], v[42:43] op_sel_hi:[0,1]
	v_pk_mul_f32 v[80:81], v[66:67], v[40:41] op_sel_hi:[0,1]
	v_pk_mul_f32 v[78:79], v[66:67], v[38:39] op_sel_hi:[0,1]
	v_pk_mul_f32 v[84:85], v[66:67], v[36:37] op_sel_hi:[0,1]
	v_pk_mul_f32 v[82:83], v[66:67], v[34:35] op_sel_hi:[0,1]
	v_pk_mul_f32 v[68:69], v[52:53], v[66:67] op_sel_hi:[1,0]
	v_pk_mul_f32 v[66:67], v[50:51], v[66:67] op_sel_hi:[1,0]
	v_sub_f32_e32 v31, v31, v32
	v_sub_f32_e32 v13, v13, v32
	v_sub_f32_e32 v120, v120, v32
	v_sub_f32_e32 v121, v121, v32
	v_sub_f32_e32 v122, v122, v32
	v_sub_f32_e32 v123, v123, v32
	s_and_b64 s[0:1], s[14:15], vcc
	s_branch .LBB1_36

.LBB1_35:
	v_mov_b64_e32 v[68:69], v[52:53]
	v_mov_b64_e32 v[60:61], v[48:49]
	v_mov_b64_e32 v[64:65], v[44:45]
	v_mov_b64_e32 v[80:81], v[40:41]
	v_mov_b64_e32 v[84:85], v[36:37]
	s_mov_b64 s[0:1], s[14:15]
	v_mov_b64_e32 v[66:67], v[50:51]
	v_mov_b64_e32 v[58:59], v[46:47]
	v_mov_b64_e32 v[62:63], v[42:43]
	v_mov_b64_e32 v[78:79], v[38:39]
	v_mov_b64_e32 v[82:83], v[34:35]

.LBB1_37:
	ds_read_b128 v[58:61], v106
	ds_read_b128 v[62:65], v106 offset:2048
	ds_read_b128 v[66:69], v105
	ds_read_b128 v[72:75], v105 offset:2048
	s_and_b32 s0, s13, s6
	s_waitcnt lgkmcnt(3)
	v_mfma_f32_16x16x32_f16 v[58:61], v[58:61], v[2:5], v[120:123]
	s_cmp_lg_u32 s0, 0
	s_waitcnt lgkmcnt(2)
	v_mfma_f32_16x16x32_f16 v[62:65], v[62:65], v[2:5], v[120:123]
	s_waitcnt lgkmcnt(1)
	v_mfma_f32_16x16x32_f16 v[68:71], v[66:69], v[6:9], v[58:61]
	s_waitcnt lgkmcnt(0)
	v_mfma_f32_16x16x32_f16 v[64:67], v[72:75], v[6:9], v[62:65]
	s_nop 0
	ds_read_b128 v[58:61], v106 offset:4096
	ds_read_b128 v[72:75], v106 offset:6144
	ds_read_b128 v[76:79], v105 offset:4096
	ds_read_b128 v[80:83], v105 offset:6144
	s_waitcnt lgkmcnt(3)
	v_mfma_f32_16x16x32_f16 v[58:61], v[58:61], v[2:5], v[120:123]
	s_waitcnt lgkmcnt(1)
	v_mfma_f32_16x16x32_f16 v[60:63], v[76:79], v[6:9], v[58:61]
	v_mfma_f32_16x16x32_f16 v[56:59], v[72:75], v[2:5], v[120:123]
	s_waitcnt lgkmcnt(0)
	v_mfma_f32_16x16x32_f16 v[56:59], v[80:83], v[6:9], v[56:59]
	s_cbranch_scc1 .LBB1_39
	v_lshrrev_b64 v[10:11], v98, v[102:103]
	v_bfe_i32 v13, v10, 0, 1
	v_bitop3_b32 v68, v68, s5, v13 bitop3:0xe4
	v_bfe_i32 v13, v10, 16, 1
	v_bitop3_b32 v64, v64, s5, v13 bitop3:0xe4
	v_bfe_i32 v13, v11, 0, 1
	v_bitop3_b32 v60, v60, s5, v13 bitop3:0xe4
	v_bfe_i32 v13, v11, 16, 1
	v_bitop3_b32 v56, v56, s5, v13 bitop3:0xe4
	v_bfe_i32 v13, v10, 1, 1
	v_bitop3_b32 v69, v69, s5, v13 bitop3:0xe4
	v_bfe_i32 v13, v10, 17, 1
	v_bitop3_b32 v65, v65, s5, v13 bitop3:0xe4
	v_bfe_i32 v13, v11, 1, 1
	v_bitop3_b32 v61, v61, s5, v13 bitop3:0xe4
	v_bfe_i32 v13, v11, 17, 1
	v_bitop3_b32 v57, v57, s5, v13 bitop3:0xe4
	v_bfe_i32 v13, v10, 2, 1
	v_bitop3_b32 v70, v70, s5, v13 bitop3:0xe4
	v_bfe_i32 v13, v10, 18, 1
	v_bitop3_b32 v66, v66, s5, v13 bitop3:0xe4
	v_bfe_i32 v13, v11, 2, 1
	v_bitop3_b32 v62, v62, s5, v13 bitop3:0xe4
	v_bfe_i32 v13, v11, 18, 1
	v_bitop3_b32 v58, v58, s5, v13 bitop3:0xe4
	v_bfe_i32 v13, v10, 3, 1
	v_bfe_i32 v10, v10, 19, 1
	v_bitop3_b32 v67, v67, s5, v10 bitop3:0xe4
	v_bfe_i32 v10, v11, 3, 1
	v_bitop3_b32 v63, v63, s5, v10 bitop3:0xe4
	v_bfe_i32 v10, v11, 19, 1
	v_bitop3_b32 v71, v71, s5, v13 bitop3:0xe4
	v_bitop3_b32 v59, v59, s5, v10 bitop3:0xe4
.LBB1_39:
	s_nop 0
	v_max3_f32 v10, v70, v71, v68
	v_max_f32_e32 v10, v10, v69
	v_max3_f32 v10, v10, v64, v65
	v_max3_f32 v10, v10, v66, v67
	v_max3_f32 v10, v10, v60, v61
	v_max3_f32 v10, v10, v62, v63
	v_max3_f32 v10, v10, v56, v57
	v_max3_f32 v10, v10, v58, v59
	v_cmp_lt_f32_e32 vcc, s7, v10
	s_or_b64 s[0:1], s[14:15], vcc
	s_cbranch_scc0 .LBB1_43
	v_and_b32_e32 v13, 64, v0
	v_xor_b32_e32 v11, 16, v0
	v_add_u32_e32 v13, 64, v13
	v_cmp_lt_i32_e32 vcc, v11, v13
	s_mov_b64 s[22:23], 0
	s_nop 0
	v_cndmask_b32_e32 v11, v0, v11, vcc
	v_lshlrev_b32_e32 v11, 2, v11
	ds_bpermute_b32 v11, v11, v10
	v_max_f32_e32 v10, v10, v10
	s_waitcnt lgkmcnt(0)
	v_max_f32_e32 v11, v11, v11
	v_max_f32_e32 v10, v10, v11
	v_mov_b32_e32 v11, v10
	s_nop 1
	v_permlane32_swap_b32_e32 v10, v11
	v_max_f32_e32 v11, v11, v11
	v_max_f32_e32 v10, v10, v10
	v_max_f32_e32 v10, v10, v11
	v_cmp_nlg_f32_e32 vcc, s5, v10
	v_cmp_lg_f32_e64 s[0:1], s5, v10
	s_and_saveexec_b64 s[24:25], s[0:1]
	v_cmp_lt_f32_e64 s[0:1], s7, v10
	s_or_b64 s[0:1], s[14:15], s[0:1]
	s_and_b64 s[22:23], s[0:1], exec
	s_or_b64 exec, exec, s[24:25]
	v_exp_f32_e64 v11, -v10
	v_cndmask_b32_e64 v10, 0, v10, s[22:23]
	v_sub_f32_e32 v120, v120, v10
	v_sub_f32_e32 v121, v121, v10
	v_sub_f32_e32 v122, v122, v10
	v_sub_f32_e32 v123, v123, v10
	s_and_b64 s[0:1], s[14:15], vcc
	v_cndmask_b32_e64 v11, v11, 1.0, s[14:15]
	v_cndmask_b32_e64 v32, 1.0, v11, s[22:23]
	v_pk_mul_f32 v[48:49], v[48:49], v[32:33] op_sel_hi:[1,0]
	v_pk_mul_f32 v[46:47], v[46:47], v[32:33] op_sel_hi:[1,0]
	v_pk_mul_f32 v[44:45], v[32:33], v[44:45] op_sel_hi:[0,1]
	v_pk_mul_f32 v[42:43], v[32:33], v[42:43] op_sel_hi:[0,1]
	v_pk_mul_f32 v[40:41], v[32:33], v[40:41] op_sel_hi:[0,1]
	v_pk_mul_f32 v[38:39], v[32:33], v[38:39] op_sel_hi:[0,1]
	v_pk_mul_f32 v[36:37], v[32:33], v[36:37] op_sel_hi:[0,1]
	v_pk_mul_f32 v[34:35], v[32:33], v[34:35] op_sel_hi:[0,1]
	v_pk_mul_f32 v[52:53], v[52:53], v[32:33] op_sel_hi:[1,0]
	v_pk_mul_f32 v[50:51], v[50:51], v[32:33] op_sel_hi:[1,0]
	v_pk_add_f32 v[68:69], v[68:69], v[10:11] op_sel_hi:[1,0] neg_lo:[0,1] neg_hi:[0,1]
	v_pk_add_f32 v[70:71], v[70:71], v[10:11] op_sel_hi:[1,0] neg_lo:[0,1] neg_hi:[0,1]
	v_pk_add_f32 v[64:65], v[64:65], v[10:11] op_sel_hi:[1,0] neg_lo:[0,1] neg_hi:[0,1]
	v_pk_add_f32 v[66:67], v[66:67], v[10:11] op_sel_hi:[1,0] neg_lo:[0,1] neg_hi:[0,1]
	v_pk_add_f32 v[60:61], v[60:61], v[10:11] op_sel_hi:[1,0] neg_lo:[0,1] neg_hi:[0,1]
	v_pk_add_f32 v[62:63], v[62:63], v[10:11] op_sel_hi:[1,0] neg_lo:[0,1] neg_hi:[0,1]
	v_pk_add_f32 v[56:57], v[56:57], v[10:11] op_sel_hi:[1,0] neg_lo:[0,1] neg_hi:[0,1]
	v_pk_add_f32 v[58:59], v[58:59], v[10:11] op_sel_hi:[1,0] neg_lo:[0,1] neg_hi:[0,1]
	s_branch .LBB1_44

.LBB1_44:
	v_exp_f32_e32 v10, v68
	v_exp_f32_e32 v11, v69
	v_exp_f32_e32 v32, v64
	v_exp_f32_e32 v13, v70
	v_exp_f32_e32 v31, v71
	v_cvt_pkrtz_f16_f32 v64, v10, v11
	v_add_u32_e32 v10, s10, v87
	ds_read_b128 v[72:75], v10 offset:8192
	ds_read_b128 v[76:79], v10 offset:10240
	v_exp_f32_e32 v33, v65
	v_exp_f32_e32 v54, v66
	v_exp_f32_e32 v55, v67
	ds_read_b128 v[80:83], v10 offset:12288
	ds_read_b128 v[106:109], v10 offset:9216
	v_cvt_pkrtz_f16_f32 v65, v13, v31
	v_cvt_pkrtz_f16_f32 v67, v54, v55
	v_cvt_pkrtz_f16_f32 v66, v32, v33
	v_exp_f32_e32 v84, v60
	v_exp_f32_e32 v85, v61
	v_exp_f32_e32 v11, v62
	s_waitcnt lgkmcnt(3)
	v_mfma_f32_16x16x32_f16 v[46:49], v[72:75], v[64:67], v[46:49]
	v_exp_f32_e32 v13, v63
	ds_read_b128 v[60:63], v10 offset:14336
	ds_read_b128 v[110:113], v10 offset:11264
	v_exp_f32_e32 v31, v56
	s_waitcnt lgkmcnt(4)
	v_mfma_f32_16x16x32_f16 v[42:45], v[76:79], v[64:67], v[42:45]
	v_exp_f32_e32 v72, v57
	ds_read_b128 v[54:57], v10 offset:13312
	v_exp_f32_e32 v73, v58
	s_waitcnt lgkmcnt(4)
	v_mfma_f32_16x16x32_f16 v[38:41], v[80:83], v[64:67], v[38:41]
	ds_read_b128 v[78:81], v10 offset:15360
	v_exp_f32_e32 v74, v59
	v_cvt_pkrtz_f16_f32 v58, v84, v85
	v_mfma_f32_16x16x32_f16 v[50:53], v[114:117], v[64:67], v[50:53]
	v_cvt_pkrtz_f16_f32 v59, v11, v13
	s_waitcnt lgkmcnt(3)
	v_mfma_f32_16x16x32_f16 v[34:37], v[60:63], v[64:67], v[34:37]
	v_cvt_pkrtz_f16_f32 v61, v73, v74
	v_cvt_pkrtz_f16_f32 v60, v31, v72
	s_nop 1
	v_mfma_f32_16x16x32_f16 v[50:53], v[114:117], v[58:61], v[50:53]
	v_mfma_f32_16x16x32_f16 v[46:49], v[106:109], v[58:61], v[46:49]
	s_waitcnt lgkmcnt(2)
	v_mfma_f32_16x16x32_f16 v[42:45], v[110:113], v[58:61], v[42:45]
	s_waitcnt lgkmcnt(1)
	v_mfma_f32_16x16x32_f16 v[38:41], v[54:57], v[58:61], v[38:41]
	s_waitcnt lgkmcnt(0)
	v_mfma_f32_16x16x32_f16 v[34:37], v[78:81], v[58:61], v[34:37]
	s_andn2_b64 vcc, exec, s[18:19]
	s_cbranch_vccnz .Lat_exit4
	s_xor_b32 s9, s9, 1
	s_lshl_b32 s10, s9, 14
	s_waitcnt vmcnt(0)
	v_or_b32_e32 v10, s10, v99
	v_mov_b64_e32 v[102:103], v[100:101]
	v_or_b32_e32 v11, s10, v90
	ds_write_b128 v10, v[22:25]
	ds_write_b128 v11, v[14:17] offset:8192
	ds_write_b128 v10, v[18:21] offset:4096
	ds_write_b128 v11, v[26:29] offset:12288
	s_mov_b64 s[14:15], s[0:1]
	s_mov_b32 s0, s16
	s_cmp_gt_i32 s11, 3
	s_cbranch_scc1 .LBB1_17
	s_branch .LBB1_20

.LBB1_46:
	v_mov_b64_e32 v[34:35], v[58:59]
	v_mov_b64_e32 v[38:39], v[62:63]
	v_mov_b64_e32 v[42:43], v[66:67]
	v_mov_b64_e32 v[46:47], v[70:71]
	v_mov_b64_e32 v[50:51], v[74:75]
	s_mov_b64 s[14:15], s[0:1]
	v_mov_b64_e32 v[36:37], v[60:61]
	v_mov_b64_e32 v[40:41], v[64:65]
	v_mov_b64_e32 v[44:45], v[68:69]
	v_mov_b64_e32 v[48:49], v[72:73]
	v_mov_b64_e32 v[52:53], v[76:77]
	s_mov_b32 s0, s16
	s_waitcnt vmcnt(0)
	v_mov_b64_e32 v[100:101], v[102:103]
	s_cmp_gt_i32 s11, 3
	s_cbranch_scc1 .LBB1_17
	s_branch .LBB1_20

	.amdhsa_kernel _Z11attn_kernelPKDF16_S0_S0_PKyPKiPDF16_
		.amdhsa_group_segment_fixed_size 36864
		.amdhsa_private_segment_fixed_size 0
		.amdhsa_kernarg_size 48
		.amdhsa_user_sgpr_count 2
		.amdhsa_user_sgpr_dispatch_ptr 0
		.amdhsa_user_sgpr_queue_ptr 0
		.amdhsa_user_sgpr_kernarg_segment_ptr 1
		.amdhsa_user_sgpr_dispatch_id 0
		.amdhsa_user_sgpr_kernarg_preload_length 0
		.amdhsa_user_sgpr_kernarg_preload_offset 0
		.amdhsa_user_sgpr_private_segment_size 0
		.amdhsa_uses_dynamic_stack 0
		.amdhsa_enable_private_segment 0
		.amdhsa_system_sgpr_workgroup_id_x 1
		.amdhsa_system_sgpr_workgroup_id_y 0
		.amdhsa_system_sgpr_workgroup_id_z 0
		.amdhsa_system_sgpr_workgroup_info 0
		.amdhsa_system_vgpr_workitem_id 0
		.amdhsa_next_free_vgpr 124
		.amdhsa_next_free_sgpr 96
		.amdhsa_accum_offset 124
		.amdhsa_reserve_vcc 1
		.amdhsa_float_round_mode_32 0
		.amdhsa_float_round_mode_16_64 0
		.amdhsa_float_denorm_mode_32 3
		.amdhsa_float_denorm_mode_16_64 3
		.amdhsa_dx10_clamp 1
		.amdhsa_ieee_mode 1
		.amdhsa_fp16_overflow 0
		.amdhsa_tg_split 0
		.amdhsa_exception_fp_ieee_invalid_op 0
		.amdhsa_exception_fp_denorm_src 0
		.amdhsa_exception_fp_ieee_div_zero 0
		.amdhsa_exception_fp_ieee_overflow 0
		.amdhsa_exception_fp_ieee_underflow 0
		.amdhsa_exception_fp_ieee_inexact 0
		.amdhsa_exception_int_div_zero 0
	.end_amdhsa_kernel

amdhsa.kernels:
  - .agpr_count:     0
    .args:
      - .actual_access:  read_only
        .address_space:  global
        .offset:         0
        .size:           8
        .value_kind:     global_buffer
      - .actual_access:  read_only
        .address_space:  global
        .offset:         8
        .size:           8
        .value_kind:     global_buffer
      - .actual_access:  read_only
        .address_space:  global
        .offset:         16
        .size:           8
        .value_kind:     global_buffer
      - .actual_access:  read_only
        .address_space:  global
        .offset:         24
        .size:           8
        .value_kind:     global_buffer
      - .actual_access:  read_only
        .address_space:  global
        .offset:         32
        .size:           8
        .value_kind:     global_buffer
      - .actual_access:  read_only
        .address_space:  global
        .offset:         40
        .size:           8
        .value_kind:     global_buffer
      - .actual_access:  write_only
        .address_space:  global
        .offset:         48
        .size:           8
        .value_kind:     global_buffer
      - .actual_access:  write_only
        .address_space:  global
        .offset:         56
        .size:           8
        .value_kind:     global_buffer
      - .actual_access:  write_only
        .address_space:  global
        .offset:         64
        .size:           8
        .value_kind:     global_buffer
      - .actual_access:  write_only
        .address_space:  global
        .offset:         72
        .size:           8
        .value_kind:     global_buffer
      - .actual_access:  write_only
        .address_space:  global
        .offset:         80
        .size:           8
        .value_kind:     global_buffer
    .group_segment_fixed_size: 16640
    .kernarg_segment_align: 8
    .kernarg_segment_size: 88
    .language:       OpenCL C
    .language_version:
      - 2
      - 0
    .max_flat_workgroup_size: 256
    .name:           _Z11prep_kernelPKfS0_S0_S0_S0_PKiPDF16_S3_S3_PyPi
    .private_segment_fixed_size: 0
    .sgpr_count:     54
    .sgpr_spill_count: 0
    .symbol:         _Z11prep_kernelPKfS0_S0_S0_S0_PKiPDF16_S3_S3_PyPi.kd
    .uniform_work_group_size: 1
    .uses_dynamic_stack: false
    .vgpr_count:     46
    .vgpr_spill_count: 0
    .wavefront_size: 64
  - .agpr_count:     0
    .args:
      - .actual_access:  read_only
        .address_space:  global
        .offset:         0
        .size:           8
        .value_kind:     global_buffer
      - .actual_access:  read_only
        .address_space:  global
        .offset:         8
        .size:           8
        .value_kind:     global_buffer
      - .actual_access:  read_only
        .address_space:  global
        .offset:         16
        .size:           8
        .value_kind:     global_buffer
      - .actual_access:  read_only
        .address_space:  global
        .offset:         24
        .size:           8
        .value_kind:     global_buffer
      - .actual_access:  read_only
        .address_space:  global
        .offset:         32
        .size:           8
        .value_kind:     global_buffer
      - .actual_access:  write_only
        .address_space:  global
        .offset:         40
        .size:           8
        .value_kind:     global_buffer
    .group_segment_fixed_size: 36864
    .kernarg_segment_align: 8
    .kernarg_segment_size: 48
    .language:       OpenCL C
    .language_version:
      - 2
      - 0
    .max_flat_workgroup_size: 256
    .name:           _Z11attn_kernelPKDF16_S0_S0_PKyPKiPDF16_
    .private_segment_fixed_size: 0
    .sgpr_count:     32
    .sgpr_spill_count: 0
    .symbol:         _Z11attn_kernelPKDF16_S0_S0_PKyPKiPDF16_.kd
    .uniform_work_group_size: 1
    .uses_dynamic_stack: false
    .vgpr_count:     124
    .vgpr_spill_count: 0
    .wavefront_size: 64
  - .agpr_count:     0
    .args:
      - .address_space:  global
        .offset:         0
        .size:           8
        .value_kind:     global_buffer
      - .address_space:  global
        .offset:         8
        .size:           8
        .value_kind:     global_buffer
      - .actual_access:  read_only
        .address_space:  global
        .offset:         16
        .size:           8
        .value_kind:     global_buffer
      - .actual_access:  read_only
        .address_space:  global
        .offset:         24
        .size:           8
        .value_kind:     global_buffer
      - .actual_access:  read_only
        .address_space:  global
        .offset:         32
        .size:           8
        .value_kind:     global_buffer
      - .actual_access:  read_only
        .address_space:  global
        .offset:         40
        .size:           8
        .value_kind:     global_buffer
      - .actual_access:  write_only
        .address_space:  global
        .offset:         48
        .size:           8
        .value_kind:     global_buffer
      - .actual_access:  write_only
        .address_space:  global
        .offset:         56
        .size:           8
        .value_kind:     global_buffer
      - .actual_access:  write_only
        .address_space:  global
        .offset:         64
        .size:           8
        .value_kind:     global_buffer
    .group_segment_fixed_size: 114688
    .kernarg_segment_align: 8
    .kernarg_segment_size: 72
    .language:       OpenCL C
    .language_version:
      - 2
      - 0
    .max_flat_workgroup_size: 512
    .name:           _Z9gemm_gldsILi256ELi192ELi4ELi2ELi2ELi4ELi8ELi0ELi4096ELi3072ELi1024EEvPKDF16_S1_PfPKfS4_PKiPDF16_S7_S7_
    .private_segment_fixed_size: 0
    .sgpr_count:     29
    .sgpr_spill_count: 0
    .symbol:         _Z9gemm_gldsILi256ELi192ELi4ELi2ELi2ELi4ELi8ELi0ELi4096ELi3072ELi1024EEvPKDF16_S1_PfPKfS4_PKiPDF16_S7_S7_.kd
    .uniform_work_group_size: 1
    .uses_dynamic_stack: false
    .vgpr_count:     214
    .vgpr_spill_count: 0
    .wavefront_size: 64
  - .agpr_count:     0
    .args:
      - .address_space:  global
        .offset:         0
        .size:           8
        .value_kind:     global_buffer
      - .address_space:  global
        .offset:         8
        .size:           8
        .value_kind:     global_buffer
      - .actual_access:  write_only
        .address_space:  global
        .offset:         16
        .size:           8
        .value_kind:     global_buffer
      - .actual_access:  read_only
        .address_space:  global
        .offset:         24
        .size:           8
        .value_kind:     global_buffer
      - .actual_access:  read_only
        .address_space:  global
        .offset:         32
        .size:           8
        .value_kind:     global_buffer
      - .actual_access:  read_only
        .address_space:  global
        .offset:         40
        .size:           8
        .value_kind:     global_buffer
      - .actual_access:  read_only
        .address_space:  global
        .offset:         48
        .size:           8
        .value_kind:     global_buffer
      - .actual_access:  read_only
        .address_space:  global
        .offset:         56
        .size:           8
        .value_kind:     global_buffer
      - .actual_access:  read_only
        .address_space:  global
        .offset:         64
        .size:           8
        .value_kind:     global_buffer
    .group_segment_fixed_size: 98304
    .kernarg_segment_align: 8
    .kernarg_segment_size: 72
    .language:       OpenCL C
    .language_version:
      - 2
      - 0
    .max_flat_workgroup_size: 512
    .name:           _Z9gemm_gldsILi128ELi128ELi4ELi2ELi3ELi8ELi4ELi1ELi4096ELi1024ELi1024EEvPKDF16_S1_PfPKfS4_PKiPDF16_S7_S7_
    .private_segment_fixed_size: 0
    .sgpr_count:     20
    .sgpr_spill_count: 0
    .symbol:         _Z9gemm_gldsILi128ELi128ELi4ELi2ELi3ELi8ELi4ELi1ELi4096ELi1024ELi1024EEvPKDF16_S1_PfPKfS4_PKiPDF16_S7_S7_.kd
    .uniform_work_group_size: 1
    .uses_dynamic_stack: false
    .vgpr_count:     92
    .vgpr_spill_count: 0
    .wavefront_size: 64
